# kernel start: each wave touches one word per 64 KiB of the expert weight buffers and the fp8 copies (address-translation warm-up), on top of best
# baseline (speedup 1.0000x reference)
; #define LANE_NOW() ({ int l_ = lane_id_now(); asm volatile("" : "+v"(l_)); l_; })
; __global__ void __launch_bounds__(NTHR, 2) fwd(Args args) {
;     ...
;     if (IN(0)) {
;         const int lane = LANE_NOW(), tid = wave * 64 + lane; (void)tid; (void)lane;
;         const int gw = bx * NWAVES + wave, NGW = NG * NWAVES;
;         constexpr int I_IN = (D / 64) * (INC / 64), I_QB = (QL / 64) * (1536 / 64), I_KVB = (KVL / 64) * (2048 / 64), I_GLU = (SSMW / 64) * (SSMW / 64), I_SQ = (D / 64) * (D / 64);
;         constexpr int I_UP = (D / 64) * (2 * FF / 64), I_DN = (FF / 64) * (D / 64);
;     ...
;         auto dec_up = [&](int it) { TItem d; int r = it; const int e = r / I_UP; r -= e * I_UP; TI_MAT8(INP(31) + (size_t)e * D * 2 * FF, D, 2 * FF, WSP(unsigned char, WS_WUP) + (size_t)e * 2 * FF * D, INP(28)); return d; };
;         auto dec_dn = [&](int it) { TItem d; int r = it; const int e = r / I_DN; r -= e * I_DN; TI_MAT8(INP(33) + (size_t)e * FF * D, FF, D, WSP(unsigned char, WS_WDN) + (size_t)e * D * FF, INP(28)); return d; };
;         auto dec_xq = [&](int it) { TItem d; int r = it; TI_MAT8(INP(24), D, D, WSP(unsigned char, WS_WXQ8), INP(22)); return d; };
;         auto dec_xo = [&](int it) { TItem d; int r = it; TI_MAT8(INP(27), D, D, WSP(unsigned char, WS_WXO8), INP(22)); return d; };
;         auto dec_16 = [&](int it) { TItem d; int r = it;
;             if (r < I_IN) { TI_MAT(INP(4), D, INC, WSP(bf16, WS_WIN), INP(22)); return d; } r -= I_IN;
;             if (r < I_QB) { TI_MAT(INP(6), QL, 1536, WSP(bf16, WS_WQB), INP(22)); return d; } r -= I_QB;
;             if (r < I_KVB) { TI_MAT(INP(8), KVL, 2048, WSP(bf16, WS_WKVB), INP(22)); return d; } r -= I_KVB;
;             if (r < I_GLU) { TI_MAT(INP(17), SSMW, SSMW, WSP(bf16, WS_WGLU), INP(22)); return d; } r -= I_GLU;
;             if (r < I_SQ) { TI_MAT(INP(25), D, D, WSP(bf16, WS_WXK), INP(22)); return d; } r -= I_SQ;
;             if (r < I_SQ) { TI_MAT(INP(26), D, D, WSP(bf16, WS_WXV), INP(22)); return d; } r -= I_SQ;
;             TI_MAT(INP(21), D, D, WSP(bf16, WS_WOUT), INP(22)); return d; };
;     ...
;         if (bx < G) { s5_setup(bx, lds, INP(9), INP(10), INP(11), INP(12), INP(13), INP(14), INP(15), WSP(bf16, WS_BTY), WSP(bf16, WS_BTS), WSP(float, WS_AP32), tid); }
;         else {
;             const int gw = (bx - G) * NWAVES + wave, NGW = (NG - G) * NWAVES, gt = (bx - G) * NTHR + tid, NGT = (NG - G) * NTHR;
.LBB0_10:
	s_waitcnt lgkmcnt(0)
	v_writelane_b32 v254, s44, 42
	s_add_u32 s88, s78, 0x37dc8000
	s_addc_u32 s87, s79, 0
	v_writelane_b32 v254, s45, 43
	v_writelane_b32 v254, s46, 44
	v_writelane_b32 v254, s47, 45
	v_writelane_b32 v254, s48, 46
	v_writelane_b32 v254, s49, 47
	v_writelane_b32 v254, s50, 48
	v_writelane_b32 v254, s51, 49
	v_writelane_b32 v254, s52, 50
	s_add_u32 s90, s78, 0x10000
	v_writelane_b32 v254, s53, 51
	s_addc_u32 s91, s79, 0
	v_writelane_b32 v254, s54, 52
	s_cmp_gt_i32 s80, 0
	v_writelane_b32 v254, s55, 53
	s_cselect_b64 s[0:1], -1, 0
	s_cmp_lt_i32 s81, 1
	v_writelane_b32 v254, s56, 54
	s_cselect_b64 s[2:3], -1, 0
	v_writelane_b32 v254, s57, 55
	s_or_b64 s[0:1], s[0:1], s[2:3]
	v_writelane_b32 v254, s58, 56
	s_and_b64 vcc, exec, s[0:1]
	v_writelane_b32 v254, s59, 57
	s_cbranch_vccnz .LBB0_264
	s_lshl_b32 s0, s92, 3
	s_add_i32 s0, s0, s89
	s_lshl_b32 s0, s0, 16
	v_mov_b32_e32 v251, s0
	v_readlane_b32 s2, v254, 56
	v_readlane_b32 s3, v254, 57
	s_nop 4
	global_load_dword v250, v251, s[2:3]
	v_add_u32_e32 v251, 0x8000000, v251
	global_load_dword v250, v251, s[2:3]
	v_add_u32_e32 v251, 0x8000000, v251
	global_load_dword v250, v251, s[2:3]
	v_add_u32_e32 v251, 0x8000000, v251
	global_load_dword v250, v251, s[2:3]
	v_add_u32_e32 v251, 0x8000000, v251
	global_load_dword v250, v251, s[2:3]
	v_add_u32_e32 v251, 0x8000000, v251
	global_load_dword v250, v251, s[2:3]
	v_add_u32_e32 v251, 0x8000000, v251
	global_load_dword v250, v251, s[2:3]
	v_add_u32_e32 v251, 0x8000000, v251
	global_load_dword v250, v251, s[2:3]
	v_mov_b32_e32 v251, s0
	v_readlane_b32 s2, v254, 4
	v_readlane_b32 s3, v254, 5
	s_nop 4
	global_load_dword v250, v251, s[2:3]
	v_add_u32_e32 v251, 0x8000000, v251
	global_load_dword v250, v251, s[2:3]
	v_add_u32_e32 v251, 0x8000000, v251
	global_load_dword v250, v251, s[2:3]
	v_add_u32_e32 v251, 0x8000000, v251
	global_load_dword v250, v251, s[2:3]
	v_mov_b32_e32 v251, s0
	s_mov_b32 s2, s88
	s_mov_b32 s3, s87
	s_nop 0
	global_load_dword v250, v251, s[2:3]
	v_add_u32_e32 v251, 0x8000000, v251
	global_load_dword v250, v251, s[2:3]
	v_add_u32_e32 v251, 0x8000000, v251
	global_load_dword v250, v251, s[2:3]
	v_mov_b32_e32 v0, 0
	s_cmp_gt_i32 s92, 63
	v_mbcnt_lo_u32_b32 v0, -1, v0
	v_mbcnt_hi_u32_b32 v134, -1, v0
	s_mov_b64 s[0:1], -1
	v_add_u32_e32 v132, s94, v134
	s_cbranch_scc0 .LBB0_22
	s_sub_i32 s3, s92, 64
	s_sub_i32 s2, s83, 64
	v_lshl_add_u32 v136, s3, 9, v132
	s_mov_b32 s0, 0x100000
	s_lshl_b32 s24, s2, 9
	v_cmp_gt_i32_e32 vcc, s0, v136
	v_ashrrev_i32_e32 v137, 31, v136
	s_and_saveexec_b64 s[0:1], vcc
	v_readlane_b32 s60, v254, 26
	v_readlane_b32 s72, v254, 38
	v_readlane_b32 s73, v254, 39
	v_readlane_b32 s61, v254, 27
	v_readlane_b32 s62, v254, 28
	v_readlane_b32 s63, v254, 29
	v_readlane_b32 s64, v254, 30
	v_readlane_b32 s65, v254, 31
	v_readlane_b32 s66, v254, 32
	v_readlane_b32 s67, v254, 33
	v_readlane_b32 s68, v254, 34
	v_readlane_b32 s69, v254, 35
	v_readlane_b32 s70, v254, 36
	v_readlane_b32 s71, v254, 37
	v_readlane_b32 s74, v254, 40
	v_readlane_b32 s75, v254, 41
	s_cbranch_execz .LBB0_15
	v_mov_b32_e32 v2, s44
	v_mov_b32_e32 v3, s45
	v_lshl_add_u64 v[0:1], v[136:137], 3, s[78:79]
	s_mov_b64 s[4:5], 0x18c28000
	s_ashr_i32 s25, s24, 31
	v_lshl_add_u64 v[0:1], v[0:1], 0, s[4:5]
	s_lshl_b64 s[4:5], s[24:25], 3
	v_lshl_add_u64 v[2:3], v[136:137], 4, v[2:3]
	s_lshl_b64 s[6:7], s[24:25], 4
	s_mov_b64 s[26:27], 0
	s_movk_i32 s25, 0x7fff
	v_mov_b32_e32 v4, 1
	v_mov_b32_e32 v5, v136
	s_mov_b32 s28, 0xfffff
